# plus: GEMM prologues issue the second DMA batch before waiting for the first (5 phases)
# baseline (speedup 1.0000x reference)
; #define PG8_STAGE2(bufoff, gbase, v0, v1) do { \
;         __builtin_amdgcn_global_load_lds((const unsigned*)((const char*)(gbase) + (v0)), (LAS unsigned*)(lds + (bufoff) + ldsw), 16, 0, 0); \
;         __builtin_amdgcn_global_load_lds((const unsigned*)((const char*)(gbase) + (v1)), (LAS unsigned*)(lds + (bufoff) + ldsw + 8192), 16, 0, 0); } while (0)
; #define PG8_STAGE(bufoff, gbase, voff) PG8_STAGE2(bufoff, gbase, (voff)[0], (voff)[1])
; #define PG8_WAIT_V(n) asm volatile("s_waitcnt vmcnt(" #n ")" ::: "memory")
; #define PG8_BAR __builtin_amdgcn_s_barrier()
; template <class Epi, class Sched, bool ALIGN_EPI, bool SP2, bool GATHER>
; DI void gemm_phase(LAS unsigned char* lds, const Gemm g, const Sched& S, const Epi& E) {
;     ...
;     PG8_STAGE(PG8_SB(0, 0), cB, voffB); PG8_STAGE(PG8_SB(0, 1), cB + hstep, voffB); PG8_STAGE2(PG8_SA(0, 0), cA, gC[0][0], gC[0][1]); PG8_STAGE2(PG8_SA(0, 1), cA + hstepA, gC[1][0], gC[1][1]);
;     if (wr == 1) PG8_BAR;
;     PG8_WAIT_V(2); PG8_BAR;
;     PG8_STAGE(PG8_SB(1, 0), cB + kstep, voffB); PG8_STAGE2(PG8_SA(1, 0), cA + kstep, gC[0][0], gC[0][1]); PG8_STAGE(PG8_SB(1, 1), cB + hstep + kstep, voffB);
;     PG8_WAIT_V(6); PG8_BAR;
.LBB0_97:
	s_mov_b64 s[28:29], 0x80
	s_and_b32 s71, s16, 3
	v_lshl_add_u64 v[10:11], v[10:11], 0, s[28:29]
	s_add_i32 m0, s67, 0x18000
	s_lshl_b32 s72, s17, 6
	s_lshl_b32 s5, s17, 13
	s_lshl_b32 s7, s71, 12
	global_load_lds_dwordx4 v[10:11], off
	v_lshl_add_u64 v[6:7], v[6:7], 0, s[28:29]
	s_add_i32 m0, s67, 0x1a000
	s_add_i32 s73, s67, 0x8000
	s_add_i32 s74, s67, 0xa000
	global_load_lds_dwordx4 v[6:7], off
	v_lshl_add_u64 v[4:5], v[4:5], 0, s[28:29]
	s_mov_b32 m0, s73
	s_add_u32 s8, s12, 0x80080
	global_load_lds_dwordx4 v[4:5], off
	v_lshl_add_u64 v[4:5], v[8:9], 0, s[28:29]
	s_mov_b32 m0, s74
	s_addc_u32 s9, s13, 0
	global_load_lds_dwordx4 v[4:5], off
	v_lshl_add_u64 v[4:5], s[8:9], 0, v[142:143]
	s_add_i32 m0, s67, 0x1c000
	v_and_b32_e32 v1, 15, v0
	global_load_lds_dwordx4 v[4:5], off
	v_lshl_add_u64 v[4:5], s[8:9], 0, v[146:147]
	s_add_i32 m0, s67, 0x1e000
	v_lshlrev_b32_e32 v6, 2, v0
	global_load_lds_dwordx4 v[4:5], off
	s_waitcnt vmcnt(8)
	s_barrier
	v_bfe_u32 v4, v0, 4, 2
	v_lshlrev_b32_e32 v149, 3, v4
	v_lshlrev_b32_e32 v4, 4, v4
	v_lshl_or_b32 v5, v1, 6, v4
	v_and_b32_e32 v6, 32, v6
	v_bitop3_b32 v5, v5, s5, v6 bitop3:0xde
	v_lshlrev_b32_e32 v7, 6, v0
	s_movk_i32 s5, 0x3c0
	v_and_or_b32 v4, v7, s5, v4
	v_lshl_or_b32 v173, s71, 5, v149
	v_bitop3_b32 v172, s7, v4, v6 bitop3:0xf6
	v_lshlrev_b32_e32 v4, 5, v173
	v_and_b32_e32 v148, 0xe00, v4
	v_lshlrev_b32_e32 v4, 1, v0
	v_and_b32_e32 v174, 32, v4
	v_lshlrev_b32_e32 v4, 9, v0
	v_and_b32_e32 v4, 0x30000, v4
	v_lshlrev_b32_e32 v6, 12, v13
	v_or3_b32 v4, v3, v4, v6
	s_cmpk_lt_u32 s22, 0x100
	v_add_u32_e32 v150, v4, v12
	v_lshlrev_b32_e32 v4, 5, v14
	s_waitcnt vmcnt(6)
	s_cselect_b64 s[30:31], -1, 0
	s_waitcnt lgkmcnt(0)
	s_add_u32 s34, s18, 0x20200000
	v_and_b32_e32 v4, 0x70000, v4
	s_addc_u32 s35, s19, 0
	v_or3_b32 v3, v3, v4, v6
	s_add_i32 s78, 0, 0x10000
	s_add_i32 s79, 0, 0x14000
	s_ashr_i32 s75, s33, 31
	s_ashr_i32 s76, s2, 31
	v_mov_b32_e32 v151, v2
	v_add_u32_e32 v152, v3, v12
	v_mov_b32_e32 v153, v2
	v_mov_b64_e32 v[154:155], 0x1080
	v_mov_b64_e32 v[156:157], 0x107f
	s_movk_i32 s77, 0x211
	v_add_u32_e32 v175, s78, v172
	v_add_u32_e32 v176, s79, v172
	v_add_u32_e32 v177, 0, v5
	s_mov_b32 s80, 0x1a200000
	s_movk_i32 s81, 0x7fff
	s_mov_b32 s82, 0x23200000
	s_mov_b64 s[36:37], 0x2000
	s_mov_b32 s83, 0x800000
	s_mov_b32 s84, 0x3f317217
	s_mov_b32 s85, 0x7f800000
	s_mov_b64 s[40:41], 0x90000
	s_mov_b64 s[42:43], 0xa0000
	s_mov_b64 s[44:45], 0xb0000
	s_mov_b64 s[46:47], 0x2200
	v_mov_b32_e32 v178, 0x3db504f3
	v_mov_b32_e32 v179, 0x41b17218
	s_mov_b32 s86, 0
	s_barrier
	s_branch .LBB0_100

; #define PG8_STAGE2(bufoff, gbase, v0, v1) do { \
;         __builtin_amdgcn_global_load_lds((const unsigned*)((const char*)(gbase) + (v0)), (LAS unsigned*)(lds + (bufoff) + ldsw), 16, 0, 0); \
;         __builtin_amdgcn_global_load_lds((const unsigned*)((const char*)(gbase) + (v1)), (LAS unsigned*)(lds + (bufoff) + ldsw + 8192), 16, 0, 0); } while (0)
; #define PG8_STAGE(bufoff, gbase, voff) PG8_STAGE2(bufoff, gbase, (voff)[0], (voff)[1])
; #define PG8_WAIT_V(n) asm volatile("s_waitcnt vmcnt(" #n ")" ::: "memory")
; #define PG8_BAR __builtin_amdgcn_s_barrier()
; template <class Epi, class Sched, bool ALIGN_EPI, bool SP2, bool GATHER>
; DI void gemm_phase(LAS unsigned char* lds, const Gemm g, const Sched& S, const Epi& E) {
;     ...
;     PG8_STAGE(PG8_SB(0, 0), cB, voffB); PG8_STAGE(PG8_SB(0, 1), cB + hstep, voffB); PG8_STAGE2(PG8_SA(0, 0), cA, gC[0][0], gC[0][1]); PG8_STAGE2(PG8_SA(0, 1), cA + hstepA, gC[1][0], gC[1][1]);
;     if (wr == 1) PG8_BAR;
;     PG8_WAIT_V(2); PG8_BAR;
;     PG8_STAGE(PG8_SB(1, 0), cB + kstep, voffB); PG8_STAGE2(PG8_SA(1, 0), cA + kstep, gC[0][0], gC[0][1]); PG8_STAGE(PG8_SB(1, 1), cB + hstep + kstep, voffB);
;     PG8_WAIT_V(6); PG8_BAR;
.LBB0_587:
	s_waitcnt lgkmcnt(0)
	s_add_u32 s12, s12, 0x23200000
	s_addc_u32 s13, s13, 0
	s_add_u32 s14, s6, 0x27200000
	s_addc_u32 s15, s7, 0
	s_add_u32 s16, s4, 0x6200000
	s_addc_u32 s17, s5, 0
	s_lshl_b32 s69, s18, 6
	s_lshl_b32 s6, s18, 13
	s_lshl_b32 s4, s19, 5
	s_mov_b64 s[18:19], 0x80
	s_and_b32 s70, s4, 0x60
	v_lshl_add_u64 v[10:11], v[10:11], 0, s[18:19]
	s_add_i32 m0, s64, 0x18000
	s_lshl_b32 s7, s70, 7
	global_load_lds_dwordx4 v[10:11], off
	v_lshl_add_u64 v[6:7], v[6:7], 0, s[18:19]
	s_add_i32 m0, s64, 0x1a000
	s_add_i32 s71, s64, 0x8000
	s_add_i32 s72, s64, 0xa000
	global_load_lds_dwordx4 v[6:7], off
	v_lshl_add_u64 v[4:5], v[4:5], 0, s[18:19]
	s_mov_b32 m0, s71
	s_add_u32 s4, s50, 0xa0080
	global_load_lds_dwordx4 v[4:5], off
	v_lshl_add_u64 v[4:5], v[8:9], 0, s[18:19]
	s_mov_b32 m0, s72
	s_addc_u32 s5, s51, 0
	global_load_lds_dwordx4 v[4:5], off
	v_lshl_add_u64 v[4:5], s[4:5], 0, v[158:159]
	s_add_i32 m0, s64, 0x1c000
	v_bfe_u32 v178, v0, 4, 2
	global_load_lds_dwordx4 v[4:5], off
	v_lshl_add_u64 v[4:5], s[4:5], 0, v[162:163]
	s_add_i32 m0, s64, 0x1e000
	v_and_b32_e32 v1, 15, v0
	global_load_lds_dwordx4 v[4:5], off
	s_waitcnt vmcnt(8)
	s_barrier
	v_lshlrev_b32_e32 v4, 4, v178
	v_lshlrev_b32_e32 v6, 2, v0
	v_lshl_or_b32 v5, v1, 6, v4
	v_and_b32_e32 v6, 32, v6
	v_bitop3_b32 v7, v5, s6, v6 bitop3:0xde
	v_lshlrev_b32_e32 v5, 6, v0
	s_movk_i32 s4, 0x3c0
	v_add_u16_e32 v3, v3, v12
	v_and_or_b32 v4, v5, s4, v4
	v_lshrrev_b16_e32 v3, 1, v3
	v_bitop3_b32 v180, s7, v4, v6 bitop3:0xf6
	s_mov_b64 s[4:5], 0xa0080
	s_waitcnt vmcnt(6)
	v_add_lshl_u32 v4, v13, v3, 1
	v_mov_b32_e32 v5, v2
	s_cmpk_lt_u32 s22, 0x100
	v_lshl_add_u64 v[164:165], v[4:5], 0, s[4:5]
	v_add_lshl_u32 v4, v14, v3, 1
	s_sext_i32_i8 s53, s20
	v_or_b32_e32 v179, s69, v1
	s_cselect_b64 s[20:21], -1, 0
	v_lshl_or_b32 v181, v178, 3, s70
	s_ashr_i32 s73, s33, 31
	v_lshl_add_u64 v[166:167], v[4:5], 0, s[4:5]
	v_mov_b64_e32 v[168:169], 0x200
	v_mov_b64_e32 v[170:171], 0x1ff
	s_mov_b64 s[22:23], 0x10000
	s_mov_b64 s[24:25], 0x20000
	s_mov_b64 s[26:27], 0x30000
	s_mov_b64 s[28:29], 0x80000
	s_mov_b64 s[30:31], 0x90000
	s_mov_b64 s[34:35], 0xb0000
	s_add_i32 s74, 0, 0x10000
	s_add_i32 s75, 0, 0x14000
	v_add_u32_e32 v182, 0, v7
	s_mov_b64 s[36:37], 0x80100
	s_mov_b64 s[40:41], 0x90100
	s_mov_b64 s[42:43], 0xa0100
	s_mov_b64 s[44:45], 0xb0100
	s_barrier
	s_branch .LBB0_590

; #define PG8_STAGE2(bufoff, gbase, v0, v1) do { \
;         __builtin_amdgcn_global_load_lds((const unsigned*)((const char*)(gbase) + (v0)), (LAS unsigned*)(lds + (bufoff) + ldsw), 16, 0, 0); \
;         __builtin_amdgcn_global_load_lds((const unsigned*)((const char*)(gbase) + (v1)), (LAS unsigned*)(lds + (bufoff) + ldsw + 8192), 16, 0, 0); } while (0)
; #define PG8_STAGE(bufoff, gbase, voff) PG8_STAGE2(bufoff, gbase, (voff)[0], (voff)[1])
; #define PG8_WAIT_V(n) asm volatile("s_waitcnt vmcnt(" #n ")" ::: "memory")
; #define PG8_BAR __builtin_amdgcn_s_barrier()
; template <class Epi, class Sched, bool ALIGN_EPI, bool SP2, bool GATHER>
; DI void gemm_phase(LAS unsigned char* lds, const Gemm g, const Sched& S, const Epi& E) {
;     ...
;     PG8_STAGE(PG8_SB(0, 0), cB, voffB); PG8_STAGE(PG8_SB(0, 1), cB + hstep, voffB); PG8_STAGE2(PG8_SA(0, 0), cA, gC[0][0], gC[0][1]); PG8_STAGE2(PG8_SA(0, 1), cA + hstepA, gC[1][0], gC[1][1]);
;     if (wr == 1) PG8_BAR;
;     PG8_WAIT_V(2); PG8_BAR;
;     PG8_STAGE(PG8_SB(1, 0), cB + kstep, voffB); PG8_STAGE2(PG8_SA(1, 0), cA + kstep, gC[0][0], gC[0][1]); PG8_STAGE(PG8_SB(1, 1), cB + hstep + kstep, voffB);
;     PG8_WAIT_V(6); PG8_BAR;
.LBB0_664:
	s_add_u32 s10, s10, 0x12200000
	s_addc_u32 s11, s11, 0
	s_lshl_b32 s4, s12, 5
	s_mov_b64 s[12:13], 0x80
	s_and_b32 s18, s4, 0x60
	v_lshl_add_u64 v[8:9], v[8:9], 0, s[12:13]
	s_add_i32 m0, s35, 0x18000
	s_lshl_b32 s17, s15, 13
	s_lshl_b32 s19, s18, 7
	global_load_lds_dwordx4 v[8:9], off
	v_lshl_add_u64 v[6:7], v[6:7], 0, s[12:13]
	s_add_i32 m0, s35, 0x1a000
	s_add_i32 s51, s35, 0x8000
	s_add_i32 s52, s35, 0xa000
	global_load_lds_dwordx4 v[6:7], off
	v_lshl_add_u64 v[2:3], v[2:3], 0, s[12:13]
	s_mov_b32 m0, s51
	s_add_u32 s4, s40, 0x80080
	global_load_lds_dwordx4 v[2:3], off
	v_lshl_add_u64 v[2:3], v[4:5], 0, s[12:13]
	s_mov_b32 m0, s52
	s_addc_u32 s5, s41, 0
	global_load_lds_dwordx4 v[2:3], off
	v_lshl_add_u64 v[2:3], s[4:5], 0, v[132:133]
	s_add_i32 m0, s35, 0x1c000
	v_lshlrev_b32_e32 v4, 2, v0
	global_load_lds_dwordx4 v[2:3], off
	v_lshl_add_u64 v[2:3], s[4:5], 0, v[136:137]
	s_add_i32 m0, s35, 0x1e000
	v_lshlrev_b32_e32 v5, 6, v0
	global_load_lds_dwordx4 v[2:3], off
	s_waitcnt vmcnt(8)
	s_barrier
	v_and_b32_e32 v2, 15, v0
	v_lshlrev_b32_e32 v3, 1, v13
	s_movk_i32 s4, 0x3c0
	v_lshl_or_b32 v1, s15, 6, v2
	v_lshl_or_b32 v2, v2, 6, v3
	v_and_b32_e32 v4, 32, v4
	v_and_or_b32 v3, v5, s4, v3
	v_bitop3_b32 v152, s19, v3, v4 bitop3:0xf6
	v_lshlrev_b32_e32 v3, 9, v0
	v_bitop3_b32 v2, v2, s17, v4 bitop3:0xde
	v_and_b32_e32 v3, 0x30000, v3
	v_lshlrev_b32_e32 v4, 12, v12
	v_or3_b32 v3, v10, v3, v4
	v_add_u32_e32 v138, v3, v11
	v_lshlrev_b32_e32 v3, 5, v14
	s_waitcnt vmcnt(6)
	s_cmpk_lt_u32 s16, 0x100
	v_and_b32_e32 v3, 0x70000, v3
	s_sext_i32_i8 s56, s14
	s_cselect_b64 s[14:15], -1, 0
	v_or3_b32 v3, v10, v3, v4
	s_add_i32 s54, 0, 0x10000
	s_add_i32 s55, 0, 0x14000
	s_ashr_i32 s53, s33, 31
	v_or_b32_e32 v153, s18, v13
	v_mov_b32_e32 v139, v133
	v_add_u32_e32 v140, v3, v11
	v_mov_b32_e32 v141, v133
	v_mov_b64_e32 v[142:143], 0x200
	v_mov_b64_e32 v[144:145], 0x1ff
	v_add_u32_e32 v154, s54, v152
	v_add_u32_e32 v155, s55, v152
	v_add_u32_e32 v156, 0, v2
	s_mov_b64 s[16:17], 0x40000
	s_mov_b64 s[18:19], 0x48000
	s_mov_b64 s[20:21], 0x50000
	s_mov_b64 s[22:23], 0x58000
	s_barrier
	s_branch .LBB0_667

; #define PG8_STAGE2(bufoff, gbase, v0, v1) do { \
;         __builtin_amdgcn_global_load_lds((const unsigned*)((const char*)(gbase) + (v0)), (LAS unsigned*)(lds + (bufoff) + ldsw), 16, 0, 0); \
;         __builtin_amdgcn_global_load_lds((const unsigned*)((const char*)(gbase) + (v1)), (LAS unsigned*)(lds + (bufoff) + ldsw + 8192), 16, 0, 0); } while (0)
; #define PG8_STAGE(bufoff, gbase, voff) PG8_STAGE2(bufoff, gbase, (voff)[0], (voff)[1])
; #define PG8_WAIT_V(n) asm volatile("s_waitcnt vmcnt(" #n ")" ::: "memory")
; #define PG8_BAR __builtin_amdgcn_s_barrier()
; template <class Epi, class Sched, bool ALIGN_EPI, bool SP2, bool GATHER>
; DI void gemm_phase(LAS unsigned char* lds, const Gemm g, const Sched& S, const Epi& E) {
;     ...
;     PG8_STAGE(PG8_SB(0, 0), cB, voffB); PG8_STAGE(PG8_SB(0, 1), cB + hstep, voffB); PG8_STAGE2(PG8_SA(0, 0), cA, gC[0][0], gC[0][1]); PG8_STAGE2(PG8_SA(0, 1), cA + hstepA, gC[1][0], gC[1][1]);
;     if (wr == 1) PG8_BAR;
;     PG8_WAIT_V(2); PG8_BAR;
;     PG8_STAGE(PG8_SB(1, 0), cB + kstep, voffB); PG8_STAGE2(PG8_SA(1, 0), cA + kstep, gC[0][0], gC[0][1]); PG8_STAGE(PG8_SB(1, 1), cB + hstep + kstep, voffB);
;     PG8_WAIT_V(6); PG8_BAR;
.LBB0_897:
	s_waitcnt lgkmcnt(0)
	s_add_u32 s10, s14, 0x2c0000
	s_addc_u32 s11, s15, 0
	s_add_u32 s12, s12, 0x2e200000
	s_mov_b64 s[14:15], 0x80
	s_addc_u32 s13, s13, 0
	s_and_b32 s20, s16, 3
	v_lshl_add_u64 v[4:5], v[4:5], 0, s[14:15]
	s_add_i32 m0, s35, 0x18000
	s_lshl_b32 s21, s19, 13
	s_lshl_b32 s22, s20, 12
	global_load_lds_dwordx4 v[4:5], off
	s_add_i32 m0, s35, 0x1a000
	s_add_u32 s16, s2, 0x12200080
	v_lshl_add_u64 v[2:3], v[2:3], 0, s[14:15]
	s_addc_u32 s17, s3, 0
	s_add_i32 s50, s35, 0x8000
	s_add_i32 s51, s35, 0xa000
	global_load_lds_dwordx4 v[2:3], off
	v_lshl_add_u64 v[2:3], s[16:17], 0, v[134:135]
	s_mov_b32 m0, s50
	s_add_u32 s2, s36, 0x80080
	global_load_lds_dwordx4 v[2:3], off
	v_lshl_add_u64 v[2:3], s[16:17], 0, v[142:143]
	s_mov_b32 m0, s51
	s_addc_u32 s3, s37, 0
	global_load_lds_dwordx4 v[2:3], off
	v_lshl_add_u64 v[2:3], s[2:3], 0, v[132:133]
	s_add_i32 m0, s35, 0x1c000
	v_lshlrev_b32_e32 v5, 2, v0
	global_load_lds_dwordx4 v[2:3], off
	v_lshl_add_u64 v[2:3], s[2:3], 0, v[130:131]
	s_add_i32 m0, s35, 0x1e000
	v_and_b32_e32 v5, 32, v5
	global_load_lds_dwordx4 v[2:3], off
	s_waitcnt vmcnt(8)
	s_barrier
	v_bfe_u32 v3, v0, 4, 2
	v_and_b32_e32 v2, 15, v0
	v_lshlrev_b32_e32 v4, 4, v3
	v_lshl_or_b32 v154, s19, 6, v2
	v_lshl_or_b32 v2, v2, 6, v4
	v_lshlrev_b32_e32 v6, 6, v0
	s_movk_i32 s2, 0x3c0
	s_waitcnt vmcnt(6)
	v_bitop3_b32 v2, v2, s21, v5 bitop3:0xde
	v_and_or_b32 v4, v6, s2, v4
	s_cmpk_lt_u32 s18, 0x100
	v_lshlrev_b32_e32 v3, 2, v3
	v_bitop3_b32 v155, s22, v4, v5 bitop3:0xf6
	s_mov_b32 s52, 0
	s_cselect_b64 s[18:19], -1, 0
	v_lshl_or_b32 v156, s20, 4, v3
	s_add_i32 s53, 0, 0x10000
	s_add_i32 s54, 0, 0x14000
	v_add_u32_e32 v157, 0, v2
	s_mov_b64 s[20:21], 0x20000
	s_mov_b64 s[22:23], 0x24000
	s_mov_b32 s55, 0x24000
	s_mov_b64 s[24:25], 0x28000
	s_mov_b32 s56, 0x28000
	s_mov_b64 s[26:27], 0x2c000
	s_mov_b32 s57, 0x2c000
	v_mov_b32_e32 v143, v134
	s_barrier
	s_branch .LBB0_900

; #define PG8_STAGE2(bufoff, gbase, v0, v1) do { \
;         __builtin_amdgcn_global_load_lds((const unsigned*)((const char*)(gbase) + (v0)), (LAS unsigned*)(lds + (bufoff) + ldsw), 16, 0, 0); \
;         __builtin_amdgcn_global_load_lds((const unsigned*)((const char*)(gbase) + (v1)), (LAS unsigned*)(lds + (bufoff) + ldsw + 8192), 16, 0, 0); } while (0)
; #define PG8_STAGE(bufoff, gbase, voff) PG8_STAGE2(bufoff, gbase, (voff)[0], (voff)[1])
; #define PG8_WAIT_V(n) asm volatile("s_waitcnt vmcnt(" #n ")" ::: "memory")
; #define PG8_BAR __builtin_amdgcn_s_barrier()
; template <class Epi, class Sched, bool ALIGN_EPI, bool SP2, bool GATHER>
; DI void gemm_phase(LAS unsigned char* lds, const Gemm g, const Sched& S, const Epi& E) {
;     ...
;     PG8_STAGE(PG8_SB(0, 0), cB, voffB); PG8_STAGE(PG8_SB(0, 1), cB + hstep, voffB); PG8_STAGE2(PG8_SA(0, 0), cA, gC[0][0], gC[0][1]); PG8_STAGE2(PG8_SA(0, 1), cA + hstepA, gC[1][0], gC[1][1]);
;     if (wr == 1) PG8_BAR;
;     PG8_WAIT_V(2); PG8_BAR;
;     PG8_STAGE(PG8_SB(1, 0), cB + kstep, voffB); PG8_STAGE2(PG8_SA(1, 0), cA + kstep, gC[0][0], gC[0][1]); PG8_STAGE(PG8_SB(1, 1), cB + hstep + kstep, voffB);
;     PG8_WAIT_V(6); PG8_BAR;
.LBB0_990:
	s_waitcnt lgkmcnt(0)
	s_add_u32 s4, s12, 0x240000
	s_addc_u32 s5, s13, 0
	s_add_u32 s6, s10, 0x280000
	s_addc_u32 s7, s11, 0
	s_add_u32 s8, s8, 0x2000000
	s_addc_u32 s9, s9, 0
	s_lshl_b32 s10, s16, 5
	s_and_b32 s16, s10, 0x60
	s_mov_b64 s[10:11], 0x80
	v_lshl_add_u64 v[8:9], v[8:9], 0, s[10:11]
	s_add_i32 m0, s27, 0x18000
	s_lshl_b32 s17, s15, 13
	s_lshl_b32 s18, s16, 7
	global_load_lds_dwordx4 v[8:9], off
	v_lshl_add_u64 v[6:7], v[6:7], 0, s[10:11]
	s_add_i32 m0, s27, 0x1a000
	s_add_i32 s46, s27, 0x8000
	s_add_i32 s47, s27, 0xa000
	global_load_lds_dwordx4 v[6:7], off
	v_lshl_add_u64 v[2:3], v[2:3], 0, s[10:11]
	s_mov_b32 m0, s46
	s_add_u32 s12, s30, 0x20080
	global_load_lds_dwordx4 v[2:3], off
	v_lshl_add_u64 v[2:3], v[4:5], 0, s[10:11]
	s_mov_b32 m0, s47
	s_addc_u32 s13, s31, 0
	global_load_lds_dwordx4 v[2:3], off
	v_lshl_add_u64 v[2:3], s[12:13], 0, v[132:133]
	s_add_i32 m0, s27, 0x1c000
	v_lshlrev_b32_e32 v4, 2, v0
	global_load_lds_dwordx4 v[2:3], off
	v_lshl_add_u64 v[2:3], s[12:13], 0, v[136:137]
	s_add_i32 m0, s27, 0x1e000
	v_lshlrev_b32_e32 v5, 6, v0
	global_load_lds_dwordx4 v[2:3], off
	s_waitcnt vmcnt(8)
	s_barrier
	v_and_b32_e32 v2, 15, v0
	v_lshlrev_b32_e32 v3, 1, v13
	s_movk_i32 s12, 0x3c0
	v_lshl_or_b32 v1, s15, 6, v2
	v_lshl_or_b32 v2, v2, 6, v3
	v_and_b32_e32 v4, 32, v4
	v_and_or_b32 v3, v5, s12, v3
	v_bitop3_b32 v152, s18, v3, v4 bitop3:0xf6
	v_lshlrev_b32_e32 v3, 7, v0
	v_bitop3_b32 v2, v2, s17, v4 bitop3:0xde
	v_and_b32_e32 v3, 0xc000, v3
	v_lshlrev_b32_e32 v4, 10, v12
	v_or3_b32 v3, v10, v3, v4
	v_add_u32_e32 v140, v3, v11
	v_lshlrev_b32_e32 v3, 3, v14
	s_waitcnt vmcnt(6)
	s_cmpk_lt_u32 s14, 0x100
	v_and_b32_e32 v3, 0x1c000, v3
	s_cselect_b64 s[12:13], -1, 0
	v_or3_b32 v3, v10, v3, v4
	s_add_i32 s48, 0, 0x10000
	s_add_i32 s49, 0, 0x14000
	v_or_b32_e32 v153, s16, v13
	v_mov_b32_e32 v141, v139
	v_add_u32_e32 v142, v3, v11
	v_mov_b32_e32 v143, v139
	v_add_u32_e32 v154, s48, v152
	v_add_u32_e32 v155, s49, v152
	v_add_u32_e32 v156, 0, v2
	s_barrier
	s_branch .LBB0_993
